# as v51 plus fp8 GEMMs use v_mfma_f32_16x16x128_f8f6f4 (implicit unit scale) instead of the scale form with both block scales 2^0: same operands, same fp8 e4m3 inputs and f32 accumulate
# speedup vs baseline: 1.0171x; 1.0171x over previous
.LBB0_841:
	ds_read_b128 v[26:29], v190
	ds_read_b128 v[30:33], v190 offset:1024
	ds_read_b128 v[18:21], v190 offset:2048
	ds_read_b128 v[22:25], v190 offset:3072
	ds_read_b128 v[10:13], v191
	ds_read_b128 v[14:17], v191 offset:1024
	ds_read_b128 v[2:5], v191 offset:2048
	ds_read_b128 v[6:9], v191 offset:3072
	s_add_u32 s24, s22, 0xfff50080
	s_addc_u32 s25, s23, -1
	s_cmp_eq_u32 s48, 40
	s_cselect_b32 s27, s9, s25
	s_cselect_b32 s26, s8, s24
	s_cselect_b32 s25, s21, s47
	s_cselect_b32 s24, s20, s46
	v_lshl_add_u64 v[218:219], s[22:23], 0, v[170:171]
	s_add_i32 m0, s31, 0xc000
	ds_read_b128 v[178:181], v192
	ds_read_b128 v[182:185], v192 offset:1024
	ds_read_b128 v[194:197], v192 offset:2048
	ds_read_b128 v[198:201], v192 offset:3072
	ds_read_b128 v[202:205], v192 offset:4096
	ds_read_b128 v[206:209], v192 offset:5120
	ds_read_b128 v[210:213], v192 offset:6144
	ds_read_b128 v[214:217], v192 offset:7168
	global_load_lds_dwordx4 v[218:219], off
	v_lshl_add_u64 v[218:219], s[22:23], 0, v[172:173]
	s_add_i32 m0, s31, 0xe000
	s_nop 0
	global_load_lds_dwordx4 v[218:219], off
	s_waitcnt vmcnt(8)
	s_waitcnt lgkmcnt(0)
	s_barrier
	s_setprio 1
	s_waitcnt lgkmcnt(0)
	v_mfma_f32_16x16x128_f8f6f4 v[158:161], v[26:33], v[178:185], v[158:161]
	v_mfma_f32_16x16x128_f8f6f4 v[154:157], v[18:25], v[178:185], v[154:157]
	v_mfma_f32_16x16x128_f8f6f4 v[142:145], v[26:33], v[194:201], v[142:145]
	v_mfma_f32_16x16x128_f8f6f4 v[138:141], v[18:25], v[194:201], v[138:141]
	v_mfma_f32_16x16x128_f8f6f4 v[126:129], v[26:33], v[202:209], v[126:129]
	v_mfma_f32_16x16x128_f8f6f4 v[122:125], v[18:25], v[202:209], v[122:125]
	v_mfma_f32_16x16x128_f8f6f4 v[110:113], v[26:33], v[210:217], v[110:113]
	v_mfma_f32_16x16x128_f8f6f4 v[106:109], v[18:25], v[210:217], v[106:109]
	s_setprio 0
	s_setprio 1
	v_mfma_f32_16x16x128_f8f6f4 v[150:153], v[10:17], v[178:185], v[150:153]
	v_mfma_f32_16x16x128_f8f6f4 v[146:149], v[2:9], v[178:185], v[146:149]
	v_mfma_f32_16x16x128_f8f6f4 v[134:137], v[10:17], v[194:201], v[134:137]
	v_mfma_f32_16x16x128_f8f6f4 v[130:133], v[2:9], v[194:201], v[130:133]
	v_mfma_f32_16x16x128_f8f6f4 v[118:121], v[10:17], v[202:209], v[118:121]
	v_mfma_f32_16x16x128_f8f6f4 v[114:117], v[2:9], v[202:209], v[114:117]
	s_setprio 2
	s_barrier
	v_mfma_f32_16x16x128_f8f6f4 v[102:105], v[10:17], v[210:217], v[102:105]
	v_mfma_f32_16x16x128_f8f6f4 v[98:101], v[2:9], v[210:217], v[98:101]
	s_setprio 0
	s_nop 0
	s_add_i32 s49, s40, s30
	v_lshl_add_u64 v[178:179], s[24:25], 0, v[164:165]
	s_mov_b32 m0, s49
	ds_read_b128 v[194:197], v192 offset:16384
	ds_read_b128 v[198:201], v192 offset:17408
	ds_read_b128 v[202:205], v192 offset:18432
	ds_read_b128 v[206:209], v192 offset:19456
	ds_read_b128 v[210:213], v192 offset:20480
	ds_read_b128 v[214:217], v192 offset:21504
	ds_read_b128 v[218:221], v192 offset:22528
	ds_read_b128 v[222:225], v192 offset:23552
	global_load_lds_dwordx4 v[178:179], off
	s_add_i32 m0, s49, 0x2000
	s_add_u32 s50, s24, 0xb0000
	v_lshl_add_u64 v[180:181], s[24:25], 0, v[168:169]
	s_addc_u32 s51, s25, 0
	s_add_i32 s49, s41, s30
	global_load_lds_dwordx4 v[180:181], off
	v_lshl_add_u64 v[182:183], s[50:51], 0, v[164:165]
	s_mov_b32 m0, s49
	v_lshl_add_u64 v[184:185], s[26:27], 0, v[166:167]
	global_load_lds_dwordx4 v[182:183], off
	v_lshl_add_u64 v[182:183], s[50:51], 0, v[168:169]
	s_add_i32 m0, s49, 0x2000
	s_nop 0
	global_load_lds_dwordx4 v[182:183], off
	v_lshl_add_u64 v[182:183], s[26:27], 0, v[162:163]
	s_mov_b32 m0, s31
	s_nop 0
	global_load_lds_dwordx4 v[182:183], off
	s_mov_b32 m0, s33
	s_nop 0
	global_load_lds_dwordx4 v[184:185], off
	s_waitcnt vmcnt(8)
	s_waitcnt lgkmcnt(0)
	s_barrier
	s_setprio 1
	s_waitcnt lgkmcnt(0)
	v_mfma_f32_16x16x128_f8f6f4 v[94:97], v[26:33], v[194:201], v[94:97]
	v_mfma_f32_16x16x128_f8f6f4 v[90:93], v[18:25], v[194:201], v[90:93]
	v_mfma_f32_16x16x128_f8f6f4 v[78:81], v[26:33], v[202:209], v[78:81]
	v_mfma_f32_16x16x128_f8f6f4 v[74:77], v[18:25], v[202:209], v[74:77]
	v_mfma_f32_16x16x128_f8f6f4 v[62:65], v[26:33], v[210:217], v[62:65]
	v_mfma_f32_16x16x128_f8f6f4 v[58:61], v[18:25], v[210:217], v[58:61]
	v_mfma_f32_16x16x128_f8f6f4 v[46:49], v[26:33], v[218:225], v[46:49]
	v_mfma_f32_16x16x128_f8f6f4 v[42:45], v[18:25], v[218:225], v[42:45]
	s_setprio 0
	s_setprio 1
	v_mfma_f32_16x16x128_f8f6f4 v[86:89], v[10:17], v[194:201], v[86:89]
	v_mfma_f32_16x16x128_f8f6f4 v[82:85], v[2:9], v[194:201], v[82:85]
	v_mfma_f32_16x16x128_f8f6f4 v[70:73], v[10:17], v[202:209], v[70:73]
	v_mfma_f32_16x16x128_f8f6f4 v[66:69], v[2:9], v[202:209], v[66:69]
	v_mfma_f32_16x16x128_f8f6f4 v[54:57], v[10:17], v[210:217], v[54:57]
	v_mfma_f32_16x16x128_f8f6f4 v[50:53], v[2:9], v[210:217], v[50:53]
	s_setprio 2
	s_barrier
	v_mfma_f32_16x16x128_f8f6f4 v[38:41], v[10:17], v[218:225], v[38:41]
	v_mfma_f32_16x16x128_f8f6f4 v[34:37], v[2:9], v[218:225], v[34:37]
	s_setprio 0
	s_nop 0
	s_add_i32 s49, 0, 0x18000
	s_add_i32 s50, 0, 0x1c000
	v_add_u32_e32 v14, s49, v188
	v_add_u32_e32 v30, s50, v188
	ds_read_b128 v[2:5], v14
	ds_read_b128 v[6:9], v14 offset:1024
	ds_read_b128 v[10:13], v14 offset:2048
	ds_read_b128 v[14:17], v14 offset:3072
	ds_read_b128 v[18:21], v30
	ds_read_b128 v[22:25], v30 offset:1024
	ds_read_b128 v[26:29], v30 offset:2048
	ds_read_b128 v[30:33], v30 offset:3072
	s_add_u32 s26, s26, 0xb0000
	s_addc_u32 s27, s27, 0
	s_mov_b32 m0, s34
	v_lshl_add_u64 v[226:227], s[26:27], 0, v[162:163]
	ds_read_b128 v[194:197], v192 offset:32768
	ds_read_b128 v[198:201], v192 offset:33792
	ds_read_b128 v[202:205], v192 offset:34816
	ds_read_b128 v[206:209], v192 offset:35840
	ds_read_b128 v[210:213], v192 offset:36864
	ds_read_b128 v[214:217], v192 offset:37888
	ds_read_b128 v[218:221], v192 offset:38912
	ds_read_b128 v[222:225], v192 offset:39936
	global_load_lds_dwordx4 v[226:227], off
	v_lshl_add_u64 v[226:227], s[26:27], 0, v[166:167]
	s_mov_b32 m0, s35
	s_nop 0
	global_load_lds_dwordx4 v[226:227], off
	s_waitcnt vmcnt(8)
	s_waitcnt lgkmcnt(0)
	s_barrier
	s_setprio 1
	s_waitcnt lgkmcnt(0)
	v_mfma_f32_16x16x128_f8f6f4 v[158:161], v[2:9], v[194:201], v[158:161]
	v_mfma_f32_16x16x128_f8f6f4 v[154:157], v[10:17], v[194:201], v[154:157]
	v_mfma_f32_16x16x128_f8f6f4 v[142:145], v[2:9], v[202:209], v[142:145]
	v_mfma_f32_16x16x128_f8f6f4 v[138:141], v[10:17], v[202:209], v[138:141]
	v_mfma_f32_16x16x128_f8f6f4 v[126:129], v[2:9], v[210:217], v[126:129]
	v_mfma_f32_16x16x128_f8f6f4 v[122:125], v[10:17], v[210:217], v[122:125]
	v_mfma_f32_16x16x128_f8f6f4 v[110:113], v[2:9], v[218:225], v[110:113]
	v_mfma_f32_16x16x128_f8f6f4 v[106:109], v[10:17], v[218:225], v[106:109]
	s_setprio 0
	s_setprio 1
	v_mfma_f32_16x16x128_f8f6f4 v[150:153], v[18:25], v[194:201], v[150:153]
	v_mfma_f32_16x16x128_f8f6f4 v[146:149], v[26:33], v[194:201], v[146:149]
	v_mfma_f32_16x16x128_f8f6f4 v[134:137], v[18:25], v[202:209], v[134:137]
	v_mfma_f32_16x16x128_f8f6f4 v[130:133], v[26:33], v[202:209], v[130:133]
	v_mfma_f32_16x16x128_f8f6f4 v[118:121], v[18:25], v[210:217], v[118:121]
	v_mfma_f32_16x16x128_f8f6f4 v[114:117], v[26:33], v[210:217], v[114:117]
	s_setprio 2
	s_barrier
	v_mfma_f32_16x16x128_f8f6f4 v[102:105], v[18:25], v[218:225], v[102:105]
	v_mfma_f32_16x16x128_f8f6f4 v[98:101], v[26:33], v[218:225], v[98:101]
	s_setprio 0
	s_nop 0
	s_add_i32 s26, s49, s30
	v_lshl_add_u64 v[178:179], v[178:179], 0, s[12:13]
	s_mov_b32 m0, s26
	ds_read_b128 v[194:197], v192 offset:49152
	ds_read_b128 v[198:201], v192 offset:50176
	ds_read_b128 v[202:205], v192 offset:51200
	ds_read_b128 v[206:209], v192 offset:52224
	ds_read_b128 v[210:213], v192 offset:53248
	ds_read_b128 v[214:217], v192 offset:54272
	ds_read_b128 v[218:221], v192 offset:55296
	ds_read_b128 v[222:225], v192 offset:56320
	global_load_lds_dwordx4 v[178:179], off
	s_add_i32 m0, s26, 0x2000
	s_add_u32 s24, s24, 0xb0080
	v_lshl_add_u64 v[178:179], v[180:181], 0, s[12:13]
	s_addc_u32 s25, s25, 0
	s_add_i32 s26, s50, s30
	global_load_lds_dwordx4 v[178:179], off
	v_lshl_add_u64 v[178:179], s[24:25], 0, v[164:165]
	s_mov_b32 m0, s26
	s_nop 0
	global_load_lds_dwordx4 v[178:179], off
	v_lshl_add_u64 v[178:179], s[24:25], 0, v[168:169]
	s_add_i32 m0, s26, 0x2000
	s_nop 0
	global_load_lds_dwordx4 v[178:179], off
	v_lshl_add_u64 v[178:179], v[182:183], 0, s[12:13]
	s_mov_b32 m0, s37
	s_nop 0
	global_load_lds_dwordx4 v[178:179], off
	v_lshl_add_u64 v[178:179], v[184:185], 0, s[12:13]
	s_mov_b32 m0, s38
	s_nop 0
	global_load_lds_dwordx4 v[178:179], off
	s_waitcnt vmcnt(8)
	s_waitcnt lgkmcnt(0)
	s_barrier
	s_setprio 1
	s_waitcnt lgkmcnt(0)
	v_mfma_f32_16x16x128_f8f6f4 v[94:97], v[2:9], v[194:201], v[94:97]
	v_mfma_f32_16x16x128_f8f6f4 v[90:93], v[10:17], v[194:201], v[90:93]
	v_mfma_f32_16x16x128_f8f6f4 v[78:81], v[2:9], v[202:209], v[78:81]
	v_mfma_f32_16x16x128_f8f6f4 v[74:77], v[10:17], v[202:209], v[74:77]
	v_mfma_f32_16x16x128_f8f6f4 v[62:65], v[2:9], v[210:217], v[62:65]
	v_mfma_f32_16x16x128_f8f6f4 v[58:61], v[10:17], v[210:217], v[58:61]
	v_mfma_f32_16x16x128_f8f6f4 v[46:49], v[2:9], v[218:225], v[46:49]
	v_mfma_f32_16x16x128_f8f6f4 v[42:45], v[10:17], v[218:225], v[42:45]
	s_setprio 0
	s_setprio 1
	v_mfma_f32_16x16x128_f8f6f4 v[86:89], v[18:25], v[194:201], v[86:89]
	v_mfma_f32_16x16x128_f8f6f4 v[82:85], v[26:33], v[194:201], v[82:85]
	v_mfma_f32_16x16x128_f8f6f4 v[70:73], v[18:25], v[202:209], v[70:73]
	v_mfma_f32_16x16x128_f8f6f4 v[66:69], v[26:33], v[202:209], v[66:69]
	v_mfma_f32_16x16x128_f8f6f4 v[54:57], v[18:25], v[210:217], v[54:57]
	v_mfma_f32_16x16x128_f8f6f4 v[50:53], v[26:33], v[210:217], v[50:53]
	s_setprio 2
	s_barrier
	v_mfma_f32_16x16x128_f8f6f4 v[38:41], v[18:25], v[218:225], v[38:41]
	v_mfma_f32_16x16x128_f8f6f4 v[34:37], v[26:33], v[218:225], v[34:37]
	s_setprio 0
	s_nop 0
	s_add_i32 s48, s48, 2
	s_add_u32 s22, s22, 0x100
	s_addc_u32 s23, s23, 0
	s_add_u32 s46, s46, 0x100
	s_addc_u32 s47, s47, 0
	s_cmp_gt_u32 s48, 41
	s_cbranch_scc0 .LBB0_841
	s_and_b64 vcc, exec, s[14:15]
	s_cbranch_vccz .LBB0_844
	s_barrier

.LBB0_1957:
	ds_read_b128 v[26:29], v194
	ds_read_b128 v[30:33], v194 offset:1024
	ds_read_b128 v[18:21], v194 offset:2048
	ds_read_b128 v[22:25], v194 offset:3072
	ds_read_b128 v[10:13], v195
	ds_read_b128 v[14:17], v195 offset:1024
	ds_read_b128 v[2:5], v195 offset:2048
	ds_read_b128 v[6:9], v195 offset:3072
	s_add_u32 s24, s58, s22
	s_addc_u32 s25, s59, s23
	s_add_u32 s26, s24, 0x50a00100
	s_addc_u32 s27, s25, 0
	s_add_u32 s72, s69, s22
	s_addc_u32 s73, s70, s23
	s_cmpk_eq_i32 s22, 0x700
	s_cselect_b64 vcc, -1, 0
	s_and_b64 s[24:25], vcc, exec
	v_cndmask_b32_e32 v168, v202, v198, vcc
	v_cndmask_b32_e32 v186, v172, v199, vcc
	v_cndmask_b32_e32 v175, v174, v200, vcc
	v_cndmask_b32_e32 v177, v176, v201, vcc
	s_cselect_b32 s27, s1, s27
	s_cselect_b32 s26, s0, s26
	s_cselect_b32 s25, s19, s73
	s_cselect_b32 s24, s68, s72
	v_lshl_add_u64 v[182:183], v[180:181], 0, s[22:23]
	s_add_i32 m0, s36, 0xc000
	ds_read_b128 v[204:207], v196
	ds_read_b128 v[208:211], v196 offset:1024
	ds_read_b128 v[212:215], v196 offset:2048
	ds_read_b128 v[216:219], v196 offset:3072
	ds_read_b128 v[220:223], v196 offset:4096
	ds_read_b128 v[224:227], v196 offset:5120
	ds_read_b128 v[228:231], v196 offset:6144
	ds_read_b128 v[232:235], v196 offset:7168
	global_load_lds_dwordx4 v[182:183], off
	v_lshl_add_u64 v[182:183], v[178:179], 0, s[22:23]
	s_add_i32 m0, s36, 0xe000
	s_nop 0
	global_load_lds_dwordx4 v[182:183], off
	s_waitcnt vmcnt(8)
	s_waitcnt lgkmcnt(0)
	s_barrier
	s_setprio 1
	s_waitcnt lgkmcnt(0)
	v_mfma_f32_16x16x128_f8f6f4 v[158:161], v[26:33], v[204:211], v[158:161]
	v_mfma_f32_16x16x128_f8f6f4 v[150:153], v[18:25], v[204:211], v[150:153]
	v_mfma_f32_16x16x128_f8f6f4 v[142:145], v[26:33], v[212:219], v[142:145]
	v_mfma_f32_16x16x128_f8f6f4 v[134:137], v[18:25], v[212:219], v[134:137]
	v_mfma_f32_16x16x128_f8f6f4 v[126:129], v[26:33], v[220:227], v[126:129]
	v_mfma_f32_16x16x128_f8f6f4 v[118:121], v[18:25], v[220:227], v[118:121]
	v_mfma_f32_16x16x128_f8f6f4 v[110:113], v[26:33], v[228:235], v[110:113]
	v_mfma_f32_16x16x128_f8f6f4 v[102:105], v[18:25], v[228:235], v[102:105]
	s_setprio 0
	s_setprio 1
	v_mfma_f32_16x16x128_f8f6f4 v[154:157], v[10:17], v[204:211], v[154:157]
	v_mfma_f32_16x16x128_f8f6f4 v[146:149], v[2:9], v[204:211], v[146:149]
	v_mfma_f32_16x16x128_f8f6f4 v[138:141], v[10:17], v[212:219], v[138:141]
	v_mfma_f32_16x16x128_f8f6f4 v[130:133], v[2:9], v[212:219], v[130:133]
	v_mfma_f32_16x16x128_f8f6f4 v[122:125], v[10:17], v[220:227], v[122:125]
	v_mfma_f32_16x16x128_f8f6f4 v[114:117], v[2:9], v[220:227], v[114:117]
	s_setprio 2
	s_barrier
	v_mfma_f32_16x16x128_f8f6f4 v[106:109], v[10:17], v[228:235], v[106:109]
	v_mfma_f32_16x16x128_f8f6f4 v[98:101], v[2:9], v[228:235], v[98:101]
	s_setprio 0
	s_nop 0
	s_add_i32 s72, s44, s28
	v_lshl_add_u64 v[182:183], s[24:25], 0, v[166:167]
	s_mov_b32 m0, s72
	ds_read_b128 v[204:207], v196 offset:16384
	ds_read_b128 v[208:211], v196 offset:17408
	ds_read_b128 v[212:215], v196 offset:18432
	ds_read_b128 v[216:219], v196 offset:19456
	ds_read_b128 v[220:223], v196 offset:20480
	ds_read_b128 v[224:227], v196 offset:21504
	ds_read_b128 v[228:231], v196 offset:22528
	ds_read_b128 v[232:235], v196 offset:23552
	global_load_lds_dwordx4 v[182:183], off
	s_add_i32 m0, s72, 0x2000
	s_add_u32 s72, s24, 0x40000
	v_lshl_add_u64 v[184:185], s[24:25], 0, v[164:165]
	s_addc_u32 s73, s25, 0
	s_add_i32 s74, s45, s28
	global_load_lds_dwordx4 v[184:185], off
	v_lshl_add_u64 v[188:189], s[72:73], 0, v[166:167]
	s_mov_b32 m0, s74
	v_mov_b32_e32 v187, v169
	global_load_lds_dwordx4 v[188:189], off
	v_lshl_add_u64 v[188:189], s[72:73], 0, v[164:165]
	s_add_i32 m0, s74, 0x2000
	s_nop 0
	global_load_lds_dwordx4 v[188:189], off
	s_mov_b32 m0, s36
	v_lshl_add_u64 v[188:189], s[26:27], 0, v[168:169]
	global_load_lds_dwordx4 v168, s[26:27]
	s_mov_b32 m0, s37
	s_nop 0
	global_load_lds_dwordx4 v186, s[26:27]
	s_waitcnt vmcnt(8)
	s_waitcnt lgkmcnt(0)
	v_lshl_add_u64 v[186:187], s[26:27], 0, v[186:187]
	s_barrier
	s_setprio 1
	s_waitcnt lgkmcnt(0)
	v_mfma_f32_16x16x128_f8f6f4 v[94:97], v[26:33], v[204:211], v[94:97]
	v_mfma_f32_16x16x128_f8f6f4 v[86:89], v[18:25], v[204:211], v[86:89]
	v_mfma_f32_16x16x128_f8f6f4 v[78:81], v[26:33], v[212:219], v[78:81]
	v_mfma_f32_16x16x128_f8f6f4 v[70:73], v[18:25], v[212:219], v[70:73]
	v_mfma_f32_16x16x128_f8f6f4 v[62:65], v[26:33], v[220:227], v[62:65]
	v_mfma_f32_16x16x128_f8f6f4 v[54:57], v[18:25], v[220:227], v[54:57]
	v_mfma_f32_16x16x128_f8f6f4 v[46:49], v[26:33], v[228:235], v[46:49]
	v_mfma_f32_16x16x128_f8f6f4 v[38:41], v[18:25], v[228:235], v[38:41]
	s_setprio 0
	s_setprio 1
	v_mfma_f32_16x16x128_f8f6f4 v[90:93], v[10:17], v[204:211], v[90:93]
	v_mfma_f32_16x16x128_f8f6f4 v[82:85], v[2:9], v[204:211], v[82:85]
	v_mfma_f32_16x16x128_f8f6f4 v[74:77], v[10:17], v[212:219], v[74:77]
	v_mfma_f32_16x16x128_f8f6f4 v[66:69], v[2:9], v[212:219], v[66:69]
	v_mfma_f32_16x16x128_f8f6f4 v[58:61], v[10:17], v[220:227], v[58:61]
	v_mfma_f32_16x16x128_f8f6f4 v[50:53], v[2:9], v[220:227], v[50:53]
	s_setprio 2
	s_barrier
	v_mfma_f32_16x16x128_f8f6f4 v[42:45], v[10:17], v[228:235], v[42:45]
	v_mfma_f32_16x16x128_f8f6f4 v[34:37], v[2:9], v[228:235], v[34:37]
	s_setprio 0
	s_nop 0
	s_add_i32 s72, 0, 0x18000
	s_add_i32 s73, 0, 0x1c000
	v_add_u32_e32 v14, s72, v192
	v_add_u32_e32 v30, s73, v192
	ds_read_b128 v[2:5], v14
	ds_read_b128 v[6:9], v14 offset:1024
	ds_read_b128 v[10:13], v14 offset:2048
	ds_read_b128 v[14:17], v14 offset:3072
	ds_read_b128 v[18:21], v30
	ds_read_b128 v[22:25], v30 offset:1024
	ds_read_b128 v[26:29], v30 offset:2048
	ds_read_b128 v[30:33], v30 offset:3072
	s_mov_b32 m0, s38
	ds_read_b128 v[204:207], v196 offset:32768
	ds_read_b128 v[208:211], v196 offset:33792
	ds_read_b128 v[212:215], v196 offset:34816
	ds_read_b128 v[216:219], v196 offset:35840
	ds_read_b128 v[220:223], v196 offset:36864
	ds_read_b128 v[224:227], v196 offset:37888
	ds_read_b128 v[228:231], v196 offset:38912
	ds_read_b128 v[232:235], v196 offset:39936
	global_load_lds_dwordx4 v175, s[26:27]
	s_mov_b32 m0, s39
	s_nop 0
	global_load_lds_dwordx4 v177, s[26:27]
	s_waitcnt vmcnt(8)
	s_waitcnt lgkmcnt(0)
	s_barrier
	s_setprio 1
	s_waitcnt lgkmcnt(0)
	v_mfma_f32_16x16x128_f8f6f4 v[158:161], v[2:9], v[204:211], v[158:161]
	v_mfma_f32_16x16x128_f8f6f4 v[150:153], v[10:17], v[204:211], v[150:153]
	v_mfma_f32_16x16x128_f8f6f4 v[142:145], v[2:9], v[212:219], v[142:145]
	v_mfma_f32_16x16x128_f8f6f4 v[134:137], v[10:17], v[212:219], v[134:137]
	v_mfma_f32_16x16x128_f8f6f4 v[126:129], v[2:9], v[220:227], v[126:129]
	v_mfma_f32_16x16x128_f8f6f4 v[118:121], v[10:17], v[220:227], v[118:121]
	v_mfma_f32_16x16x128_f8f6f4 v[110:113], v[2:9], v[228:235], v[110:113]
	v_mfma_f32_16x16x128_f8f6f4 v[102:105], v[10:17], v[228:235], v[102:105]
	s_setprio 0
	s_setprio 1
	v_mfma_f32_16x16x128_f8f6f4 v[154:157], v[18:25], v[204:211], v[154:157]
	v_mfma_f32_16x16x128_f8f6f4 v[146:149], v[26:33], v[204:211], v[146:149]
	v_mfma_f32_16x16x128_f8f6f4 v[138:141], v[18:25], v[212:219], v[138:141]
	v_mfma_f32_16x16x128_f8f6f4 v[130:133], v[26:33], v[212:219], v[130:133]
	v_mfma_f32_16x16x128_f8f6f4 v[122:125], v[18:25], v[220:227], v[122:125]
	v_mfma_f32_16x16x128_f8f6f4 v[114:117], v[26:33], v[220:227], v[114:117]
	s_setprio 2
	s_barrier
	v_mfma_f32_16x16x128_f8f6f4 v[106:109], v[18:25], v[228:235], v[106:109]
	v_mfma_f32_16x16x128_f8f6f4 v[98:101], v[26:33], v[228:235], v[98:101]
	s_setprio 0
	s_nop 0
	s_add_i32 s26, s72, s28
	v_lshl_add_u64 v[182:183], v[182:183], 0, s[10:11]
	s_mov_b32 m0, s26
	ds_read_b128 v[204:207], v196 offset:49152
	ds_read_b128 v[208:211], v196 offset:50176
	ds_read_b128 v[212:215], v196 offset:51200
	ds_read_b128 v[216:219], v196 offset:52224
	ds_read_b128 v[220:223], v196 offset:53248
	ds_read_b128 v[224:227], v196 offset:54272
	ds_read_b128 v[228:231], v196 offset:55296
	ds_read_b128 v[232:235], v196 offset:56320
	global_load_lds_dwordx4 v[182:183], off
	s_add_i32 m0, s26, 0x2000
	s_add_u32 s24, s24, 0x40080
	v_lshl_add_u64 v[182:183], v[184:185], 0, s[10:11]
	s_addc_u32 s25, s25, 0
	s_add_i32 s26, s73, s28
	global_load_lds_dwordx4 v[182:183], off
	v_lshl_add_u64 v[182:183], s[24:25], 0, v[166:167]
	s_mov_b32 m0, s26
	s_nop 0
	global_load_lds_dwordx4 v[182:183], off
	v_lshl_add_u64 v[182:183], s[24:25], 0, v[164:165]
	s_add_i32 m0, s26, 0x2000
	s_nop 0
	global_load_lds_dwordx4 v[182:183], off
	v_lshl_add_u64 v[182:183], v[188:189], 0, s[10:11]
	s_mov_b32 m0, s40
	s_nop 0
	global_load_lds_dwordx4 v[182:183], off
	v_lshl_add_u64 v[182:183], v[186:187], 0, s[10:11]
	s_mov_b32 m0, s41
	s_nop 0
	global_load_lds_dwordx4 v[182:183], off
	s_waitcnt vmcnt(8)
	s_waitcnt lgkmcnt(0)
	s_barrier
	s_setprio 1
	s_waitcnt lgkmcnt(0)
	v_mfma_f32_16x16x128_f8f6f4 v[94:97], v[2:9], v[204:211], v[94:97]
	v_mfma_f32_16x16x128_f8f6f4 v[86:89], v[10:17], v[204:211], v[86:89]
	v_mfma_f32_16x16x128_f8f6f4 v[78:81], v[2:9], v[212:219], v[78:81]
	v_mfma_f32_16x16x128_f8f6f4 v[70:73], v[10:17], v[212:219], v[70:73]
	v_mfma_f32_16x16x128_f8f6f4 v[62:65], v[2:9], v[220:227], v[62:65]
	v_mfma_f32_16x16x128_f8f6f4 v[54:57], v[10:17], v[220:227], v[54:57]
	v_mfma_f32_16x16x128_f8f6f4 v[46:49], v[2:9], v[228:235], v[46:49]
	v_mfma_f32_16x16x128_f8f6f4 v[38:41], v[10:17], v[228:235], v[38:41]
	s_setprio 0
	s_setprio 1
	v_mfma_f32_16x16x128_f8f6f4 v[90:93], v[18:25], v[204:211], v[90:93]
	v_mfma_f32_16x16x128_f8f6f4 v[82:85], v[26:33], v[204:211], v[82:85]
	v_mfma_f32_16x16x128_f8f6f4 v[74:77], v[18:25], v[212:219], v[74:77]
	v_mfma_f32_16x16x128_f8f6f4 v[66:69], v[26:33], v[212:219], v[66:69]
	v_mfma_f32_16x16x128_f8f6f4 v[58:61], v[18:25], v[220:227], v[58:61]
	v_mfma_f32_16x16x128_f8f6f4 v[50:53], v[26:33], v[220:227], v[50:53]
	s_setprio 2
	s_barrier
	v_mfma_f32_16x16x128_f8f6f4 v[42:45], v[18:25], v[228:235], v[42:45]
	v_mfma_f32_16x16x128_f8f6f4 v[34:37], v[26:33], v[228:235], v[34:37]
	s_setprio 0
	s_nop 0
	s_add_i32 s71, s71, 2
	s_add_u32 s22, s22, 0x100
	s_addc_u32 s23, s23, 0
	s_cmp_gt_u32 s71, 13
	s_cbranch_scc0 .LBB0_1957
	s_and_b64 vcc, exec, s[14:15]
	s_cbranch_vccz .LBB0_1960
	s_barrier

.LBB0_2038:
	ds_read_b128 v[26:29], v200
	ds_read_b128 v[30:33], v200 offset:1024
	ds_read_b128 v[18:21], v200 offset:2048
	ds_read_b128 v[22:25], v200 offset:3072
	ds_read_b128 v[10:13], v201
	ds_read_b128 v[14:17], v201 offset:1024
	ds_read_b128 v[2:5], v201 offset:2048
	ds_read_b128 v[6:9], v201 offset:3072
	s_add_u32 s38, s36, 0xfff20080
	s_addc_u32 s39, s37, -1
	s_cmp_eq_u32 s79, 52
	s_cselect_b64 vcc, -1, 0
	s_cselect_b32 s39, s7, s39
	s_cselect_b32 s38, s6, s38
	v_cndmask_b32_e32 v183, v181, v179, vcc
	v_cndmask_b32_e32 v182, v180, v178, vcc
	v_lshl_add_u64 v[228:229], s[36:37], 0, v[172:173]
	s_add_i32 m0, s60, 0xc000
	ds_read_b128 v[184:187], v202
	ds_read_b128 v[188:191], v202 offset:1024
	ds_read_b128 v[204:207], v202 offset:2048
	ds_read_b128 v[208:211], v202 offset:3072
	ds_read_b128 v[212:215], v202 offset:4096
	ds_read_b128 v[216:219], v202 offset:5120
	ds_read_b128 v[220:223], v202 offset:6144
	ds_read_b128 v[224:227], v202 offset:7168
	global_load_lds_dwordx4 v[228:229], off
	v_lshl_add_u64 v[228:229], s[36:37], 0, v[174:175]
	s_add_i32 m0, s60, 0xe000
	s_nop 0
	global_load_lds_dwordx4 v[228:229], off
	s_waitcnt vmcnt(8)
	s_waitcnt lgkmcnt(0)
	s_barrier
	s_setprio 1
	s_waitcnt lgkmcnt(0)
	v_mfma_f32_16x16x128_f8f6f4 v[158:161], v[26:33], v[184:191], v[158:161]
	v_mfma_f32_16x16x128_f8f6f4 v[154:157], v[18:25], v[184:191], v[154:157]
	v_mfma_f32_16x16x128_f8f6f4 v[150:153], v[26:33], v[204:211], v[150:153]
	v_mfma_f32_16x16x128_f8f6f4 v[142:145], v[18:25], v[204:211], v[142:145]
	v_mfma_f32_16x16x128_f8f6f4 v[134:137], v[26:33], v[212:219], v[134:137]
	v_mfma_f32_16x16x128_f8f6f4 v[126:129], v[18:25], v[212:219], v[126:129]
	v_mfma_f32_16x16x128_f8f6f4 v[118:121], v[26:33], v[220:227], v[118:121]
	v_mfma_f32_16x16x128_f8f6f4 v[110:113], v[18:25], v[220:227], v[110:113]
	s_setprio 0
	s_setprio 1
	v_mfma_f32_16x16x128_f8f6f4 v[146:149], v[10:17], v[184:191], v[146:149]
	v_mfma_f32_16x16x128_f8f6f4 v[138:141], v[2:9], v[184:191], v[138:141]
	v_mfma_f32_16x16x128_f8f6f4 v[130:133], v[10:17], v[204:211], v[130:133]
	v_mfma_f32_16x16x128_f8f6f4 v[122:125], v[2:9], v[204:211], v[122:125]
	v_mfma_f32_16x16x128_f8f6f4 v[114:117], v[10:17], v[212:219], v[114:117]
	v_mfma_f32_16x16x128_f8f6f4 v[106:109], v[2:9], v[212:219], v[106:109]
	s_setprio 2
	s_barrier
	v_mfma_f32_16x16x128_f8f6f4 v[102:105], v[10:17], v[220:227], v[102:105]
	v_mfma_f32_16x16x128_f8f6f4 v[98:101], v[2:9], v[220:227], v[98:101]
	s_setprio 0
	s_nop 0
	s_add_i32 s80, s69, s25
	v_lshl_add_u64 v[184:185], v[182:183], 0, v[170:171]
	s_mov_b32 m0, s80
	ds_read_b128 v[204:207], v202 offset:16384
	ds_read_b128 v[208:211], v202 offset:17408
	ds_read_b128 v[212:215], v202 offset:18432
	ds_read_b128 v[216:219], v202 offset:19456
	ds_read_b128 v[220:223], v202 offset:20480
	ds_read_b128 v[224:227], v202 offset:21504
	ds_read_b128 v[228:231], v202 offset:22528
	ds_read_b128 v[232:235], v202 offset:23552
	global_load_lds_dwordx4 v[184:185], off
	v_lshl_add_u64 v[186:187], v[182:183], 0, v[168:169]
	s_add_i32 m0, s80, 0x2000
	v_lshl_add_u64 v[188:189], v[182:183], 0, s[10:11]
	s_add_i32 s80, s70, s25
	global_load_lds_dwordx4 v[186:187], off
	v_lshl_add_u64 v[190:191], v[188:189], 0, v[170:171]
	s_mov_b32 m0, s80
	v_lshl_add_u64 v[188:189], v[188:189], 0, v[168:169]
	global_load_lds_dwordx4 v[190:191], off
	s_add_i32 m0, s80, 0x2000
	v_lshl_add_u64 v[190:191], s[38:39], 0, v[166:167]
	global_load_lds_dwordx4 v[188:189], off
	v_lshl_add_u64 v[188:189], s[38:39], 0, v[164:165]
	s_mov_b32 m0, s60
	s_nop 0
	global_load_lds_dwordx4 v[188:189], off
	s_mov_b32 m0, s61
	s_nop 0
	global_load_lds_dwordx4 v[190:191], off
	s_waitcnt vmcnt(8)
	s_waitcnt lgkmcnt(0)
	s_barrier
	s_setprio 1
	s_waitcnt lgkmcnt(0)
	v_mfma_f32_16x16x128_f8f6f4 v[94:97], v[26:33], v[204:211], v[94:97]
	v_mfma_f32_16x16x128_f8f6f4 v[90:93], v[18:25], v[204:211], v[90:93]
	v_mfma_f32_16x16x128_f8f6f4 v[86:89], v[26:33], v[212:219], v[86:89]
	v_mfma_f32_16x16x128_f8f6f4 v[78:81], v[18:25], v[212:219], v[78:81]
	v_mfma_f32_16x16x128_f8f6f4 v[70:73], v[26:33], v[220:227], v[70:73]
	v_mfma_f32_16x16x128_f8f6f4 v[62:65], v[18:25], v[220:227], v[62:65]
	v_mfma_f32_16x16x128_f8f6f4 v[54:57], v[26:33], v[228:235], v[54:57]
	v_mfma_f32_16x16x128_f8f6f4 v[46:49], v[18:25], v[228:235], v[46:49]
	s_setprio 0
	s_setprio 1
	v_mfma_f32_16x16x128_f8f6f4 v[82:85], v[10:17], v[204:211], v[82:85]
	v_mfma_f32_16x16x128_f8f6f4 v[74:77], v[2:9], v[204:211], v[74:77]
	v_mfma_f32_16x16x128_f8f6f4 v[66:69], v[10:17], v[212:219], v[66:69]
	v_mfma_f32_16x16x128_f8f6f4 v[58:61], v[2:9], v[212:219], v[58:61]
	v_mfma_f32_16x16x128_f8f6f4 v[50:53], v[10:17], v[220:227], v[50:53]
	v_mfma_f32_16x16x128_f8f6f4 v[42:45], v[2:9], v[220:227], v[42:45]
	s_setprio 2
	s_barrier
	v_mfma_f32_16x16x128_f8f6f4 v[38:41], v[10:17], v[228:235], v[38:41]
	v_mfma_f32_16x16x128_f8f6f4 v[34:37], v[2:9], v[228:235], v[34:37]
	s_setprio 0
	s_nop 0
	s_add_i32 s80, 0, 0x18000
	s_add_i32 s81, 0, 0x1c000
	v_add_u32_e32 v14, s80, v198
	v_add_u32_e32 v30, s81, v198
	ds_read_b128 v[2:5], v14
	ds_read_b128 v[6:9], v14 offset:1024
	ds_read_b128 v[10:13], v14 offset:2048
	ds_read_b128 v[14:17], v14 offset:3072
	ds_read_b128 v[18:21], v30
	ds_read_b128 v[22:25], v30 offset:1024
	ds_read_b128 v[26:29], v30 offset:2048
	ds_read_b128 v[30:33], v30 offset:3072
	s_add_u32 s38, s38, 0xe0000
	s_addc_u32 s39, s39, 0
	s_mov_b32 m0, s62
	v_lshl_add_u64 v[236:237], s[38:39], 0, v[164:165]
	ds_read_b128 v[204:207], v202 offset:32768
	ds_read_b128 v[208:211], v202 offset:33792
	ds_read_b128 v[212:215], v202 offset:34816
	ds_read_b128 v[216:219], v202 offset:35840
	ds_read_b128 v[220:223], v202 offset:36864
	ds_read_b128 v[224:227], v202 offset:37888
	ds_read_b128 v[228:231], v202 offset:38912
	ds_read_b128 v[232:235], v202 offset:39936
	global_load_lds_dwordx4 v[236:237], off
	v_lshl_add_u64 v[236:237], s[38:39], 0, v[166:167]
	s_mov_b32 m0, s63
	s_nop 0
	global_load_lds_dwordx4 v[236:237], off
	s_waitcnt vmcnt(8)
	s_waitcnt lgkmcnt(0)
	s_barrier
	s_setprio 1
	s_waitcnt lgkmcnt(0)
	v_mfma_f32_16x16x128_f8f6f4 v[158:161], v[2:9], v[204:211], v[158:161]
	v_mfma_f32_16x16x128_f8f6f4 v[154:157], v[10:17], v[204:211], v[154:157]
	v_mfma_f32_16x16x128_f8f6f4 v[150:153], v[2:9], v[212:219], v[150:153]
	v_mfma_f32_16x16x128_f8f6f4 v[142:145], v[10:17], v[212:219], v[142:145]
	v_mfma_f32_16x16x128_f8f6f4 v[134:137], v[2:9], v[220:227], v[134:137]
	v_mfma_f32_16x16x128_f8f6f4 v[126:129], v[10:17], v[220:227], v[126:129]
	v_mfma_f32_16x16x128_f8f6f4 v[118:121], v[2:9], v[228:235], v[118:121]
	v_mfma_f32_16x16x128_f8f6f4 v[110:113], v[10:17], v[228:235], v[110:113]
	s_setprio 0
	s_setprio 1
	v_mfma_f32_16x16x128_f8f6f4 v[146:149], v[18:25], v[204:211], v[146:149]
	v_mfma_f32_16x16x128_f8f6f4 v[138:141], v[26:33], v[204:211], v[138:141]
	v_mfma_f32_16x16x128_f8f6f4 v[130:133], v[18:25], v[212:219], v[130:133]
	v_mfma_f32_16x16x128_f8f6f4 v[122:125], v[26:33], v[212:219], v[122:125]
	v_mfma_f32_16x16x128_f8f6f4 v[114:117], v[18:25], v[220:227], v[114:117]
	v_mfma_f32_16x16x128_f8f6f4 v[106:109], v[26:33], v[220:227], v[106:109]
	s_setprio 2
	s_barrier
	v_mfma_f32_16x16x128_f8f6f4 v[102:105], v[18:25], v[228:235], v[102:105]
	v_mfma_f32_16x16x128_f8f6f4 v[98:101], v[26:33], v[228:235], v[98:101]
	s_setprio 0
	s_nop 0
	s_add_i32 s38, s80, s25
	v_lshl_add_u64 v[184:185], v[184:185], 0, s[16:17]
	s_mov_b32 m0, s38
	ds_read_b128 v[204:207], v202 offset:49152
	ds_read_b128 v[208:211], v202 offset:50176
	ds_read_b128 v[212:215], v202 offset:51200
	ds_read_b128 v[216:219], v202 offset:52224
	ds_read_b128 v[220:223], v202 offset:53248
	ds_read_b128 v[224:227], v202 offset:54272
	ds_read_b128 v[228:231], v202 offset:55296
	ds_read_b128 v[232:235], v202 offset:56320
	global_load_lds_dwordx4 v[184:185], off
	v_lshl_add_u64 v[184:185], v[186:187], 0, s[16:17]
	s_add_i32 m0, s38, 0x2000
	v_lshl_add_u64 v[182:183], v[182:183], 0, s[18:19]
	s_add_i32 s38, s81, s25
	global_load_lds_dwordx4 v[184:185], off
	v_lshl_add_u64 v[184:185], v[182:183], 0, v[170:171]
	s_mov_b32 m0, s38
	v_lshl_add_u64 v[182:183], v[182:183], 0, v[168:169]
	global_load_lds_dwordx4 v[184:185], off
	s_add_i32 m0, s38, 0x2000
	s_nop 0
	global_load_lds_dwordx4 v[182:183], off
	v_lshl_add_u64 v[182:183], v[188:189], 0, s[16:17]
	s_mov_b32 m0, s66
	s_nop 0
	global_load_lds_dwordx4 v[182:183], off
	v_lshl_add_u64 v[182:183], v[190:191], 0, s[16:17]
	s_mov_b32 m0, s67
	s_nop 0
	global_load_lds_dwordx4 v[182:183], off
	s_waitcnt vmcnt(8)
	s_waitcnt lgkmcnt(0)
	s_barrier
	s_setprio 1
	s_waitcnt lgkmcnt(0)
	v_mfma_f32_16x16x128_f8f6f4 v[94:97], v[2:9], v[204:211], v[94:97]
	v_mfma_f32_16x16x128_f8f6f4 v[90:93], v[10:17], v[204:211], v[90:93]
	v_mfma_f32_16x16x128_f8f6f4 v[86:89], v[2:9], v[212:219], v[86:89]
	v_mfma_f32_16x16x128_f8f6f4 v[78:81], v[10:17], v[212:219], v[78:81]
	v_mfma_f32_16x16x128_f8f6f4 v[70:73], v[2:9], v[220:227], v[70:73]
	v_mfma_f32_16x16x128_f8f6f4 v[62:65], v[10:17], v[220:227], v[62:65]
	v_mfma_f32_16x16x128_f8f6f4 v[54:57], v[2:9], v[228:235], v[54:57]
	v_mfma_f32_16x16x128_f8f6f4 v[46:49], v[10:17], v[228:235], v[46:49]
	s_setprio 0
	s_setprio 1
	v_mfma_f32_16x16x128_f8f6f4 v[82:85], v[18:25], v[204:211], v[82:85]
	v_mfma_f32_16x16x128_f8f6f4 v[74:77], v[26:33], v[204:211], v[74:77]
	v_mfma_f32_16x16x128_f8f6f4 v[66:69], v[18:25], v[212:219], v[66:69]
	v_mfma_f32_16x16x128_f8f6f4 v[58:61], v[26:33], v[212:219], v[58:61]
	v_mfma_f32_16x16x128_f8f6f4 v[50:53], v[18:25], v[220:227], v[50:53]
	v_mfma_f32_16x16x128_f8f6f4 v[42:45], v[26:33], v[220:227], v[42:45]
	s_setprio 2
	s_barrier
	v_mfma_f32_16x16x128_f8f6f4 v[38:41], v[18:25], v[228:235], v[38:41]
	v_mfma_f32_16x16x128_f8f6f4 v[34:37], v[26:33], v[228:235], v[34:37]
	s_setprio 0
	s_nop 0
	s_add_i32 s79, s79, 2
	s_add_u32 s36, s36, 0x100
	s_addc_u32 s37, s37, 0
	s_cmp_gt_u32 s79, 53
	v_lshl_add_u64 v[180:181], v[180:181], 0, s[22:23]
	s_cbranch_scc0 .LBB0_2038
	s_and_b64 vcc, exec, s[20:21]
	s_cbranch_vccz .LBB0_2041
	s_barrier

.LBB0_2058:
	ds_read_b128 v[26:29], v1
	ds_read_b128 v[30:33], v1 offset:1024
	ds_read_b128 v[18:21], v1 offset:2048
	ds_read_b128 v[22:25], v1 offset:3072
	ds_read_b128 v[10:13], v190
	ds_read_b128 v[14:17], v190 offset:1024
	ds_read_b128 v[2:5], v190 offset:2048
	ds_read_b128 v[6:9], v190 offset:3072
	s_add_i32 s25, s28, 2
	s_add_u32 s80, s26, 0xfff20080
	s_addc_u32 s29, s27, -1
	s_cmp_eq_u32 s69, s28
	s_cselect_b32 s28, s6, s80
	s_cselect_b64 vcc, -1, 0
	s_cselect_b32 s29, s7, s29
	v_cndmask_b32_e32 v179, v177, v175, vcc
	v_cndmask_b32_e32 v178, v176, v174, vcc
	v_lshl_add_u64 v[218:219], s[26:27], 0, v[168:169]
	s_add_i32 m0, s60, 0xc000
	ds_read_b128 v[180:183], v191
	ds_read_b128 v[184:187], v191 offset:1024
	ds_read_b128 v[194:197], v191 offset:2048
	ds_read_b128 v[198:201], v191 offset:3072
	ds_read_b128 v[202:205], v191 offset:4096
	ds_read_b128 v[206:209], v191 offset:5120
	ds_read_b128 v[210:213], v191 offset:6144
	ds_read_b128 v[214:217], v191 offset:7168
	global_load_lds_dwordx4 v[218:219], off
	v_lshl_add_u64 v[218:219], s[26:27], 0, v[170:171]
	s_add_i32 m0, s60, 0xe000
	s_nop 0
	global_load_lds_dwordx4 v[218:219], off
	s_waitcnt vmcnt(8)
	s_waitcnt lgkmcnt(0)
	s_barrier
	s_setprio 1
	s_waitcnt lgkmcnt(0)
	v_mfma_f32_16x16x128_f8f6f4 v[158:161], v[26:33], v[180:187], v[158:161]
	v_mfma_f32_16x16x128_f8f6f4 v[154:157], v[18:25], v[180:187], v[154:157]
	v_mfma_f32_16x16x128_f8f6f4 v[150:153], v[26:33], v[194:201], v[150:153]
	v_mfma_f32_16x16x128_f8f6f4 v[142:145], v[18:25], v[194:201], v[142:145]
	v_mfma_f32_16x16x128_f8f6f4 v[134:137], v[26:33], v[202:209], v[134:137]
	v_mfma_f32_16x16x128_f8f6f4 v[126:129], v[18:25], v[202:209], v[126:129]
	v_mfma_f32_16x16x128_f8f6f4 v[118:121], v[26:33], v[210:217], v[118:121]
	v_mfma_f32_16x16x128_f8f6f4 v[110:113], v[18:25], v[210:217], v[110:113]
	s_setprio 0
	s_setprio 1
	v_mfma_f32_16x16x128_f8f6f4 v[146:149], v[10:17], v[180:187], v[146:149]
	v_mfma_f32_16x16x128_f8f6f4 v[138:141], v[2:9], v[180:187], v[138:141]
	v_mfma_f32_16x16x128_f8f6f4 v[130:133], v[10:17], v[194:201], v[130:133]
	v_mfma_f32_16x16x128_f8f6f4 v[122:125], v[2:9], v[194:201], v[122:125]
	v_mfma_f32_16x16x128_f8f6f4 v[114:117], v[10:17], v[202:209], v[114:117]
	v_mfma_f32_16x16x128_f8f6f4 v[106:109], v[2:9], v[202:209], v[106:109]
	s_setprio 2
	s_barrier
	v_mfma_f32_16x16x128_f8f6f4 v[102:105], v[10:17], v[210:217], v[102:105]
	v_mfma_f32_16x16x128_f8f6f4 v[98:101], v[2:9], v[210:217], v[98:101]
	s_setprio 0
	s_nop 0
	s_add_i32 s80, s71, s34
	v_lshl_add_u64 v[180:181], v[178:179], 0, v[164:165]
	s_mov_b32 m0, s80
	ds_read_b128 v[194:197], v191 offset:16384
	ds_read_b128 v[198:201], v191 offset:17408
	ds_read_b128 v[202:205], v191 offset:18432
	ds_read_b128 v[206:209], v191 offset:19456
	ds_read_b128 v[210:213], v191 offset:20480
	ds_read_b128 v[214:217], v191 offset:21504
	ds_read_b128 v[218:221], v191 offset:22528
	ds_read_b128 v[222:225], v191 offset:23552
	global_load_lds_dwordx4 v[180:181], off
	v_lshl_add_u64 v[182:183], v[178:179], 0, v[166:167]
	s_add_i32 m0, s80, 0x2000
	v_lshl_add_u64 v[184:185], v[178:179], 0, s[10:11]
	s_add_i32 s80, s72, s34
	global_load_lds_dwordx4 v[182:183], off
	v_lshl_add_u64 v[186:187], v[184:185], 0, v[164:165]
	s_mov_b32 m0, s80
	v_lshl_add_u64 v[184:185], v[184:185], 0, v[166:167]
	global_load_lds_dwordx4 v[186:187], off
	s_add_i32 m0, s80, 0x2000
	v_lshl_add_u64 v[186:187], s[28:29], 0, v[166:167]
	global_load_lds_dwordx4 v[184:185], off
	v_lshl_add_u64 v[184:185], s[28:29], 0, v[164:165]
	s_mov_b32 m0, s60
	s_nop 0
	global_load_lds_dwordx4 v[184:185], off
	s_mov_b32 m0, s61
	s_nop 0
	global_load_lds_dwordx4 v[186:187], off
	s_waitcnt vmcnt(8)
	s_waitcnt lgkmcnt(0)
	s_barrier
	s_setprio 1
	s_waitcnt lgkmcnt(0)
	v_mfma_f32_16x16x128_f8f6f4 v[94:97], v[26:33], v[194:201], v[94:97]
	v_mfma_f32_16x16x128_f8f6f4 v[90:93], v[18:25], v[194:201], v[90:93]
	v_mfma_f32_16x16x128_f8f6f4 v[86:89], v[26:33], v[202:209], v[86:89]
	v_mfma_f32_16x16x128_f8f6f4 v[78:81], v[18:25], v[202:209], v[78:81]
	v_mfma_f32_16x16x128_f8f6f4 v[70:73], v[26:33], v[210:217], v[70:73]
	v_mfma_f32_16x16x128_f8f6f4 v[62:65], v[18:25], v[210:217], v[62:65]
	v_mfma_f32_16x16x128_f8f6f4 v[54:57], v[26:33], v[218:225], v[54:57]
	v_mfma_f32_16x16x128_f8f6f4 v[46:49], v[18:25], v[218:225], v[46:49]
	s_setprio 0
	s_setprio 1
	v_mfma_f32_16x16x128_f8f6f4 v[82:85], v[10:17], v[194:201], v[82:85]
	v_mfma_f32_16x16x128_f8f6f4 v[74:77], v[2:9], v[194:201], v[74:77]
	v_mfma_f32_16x16x128_f8f6f4 v[66:69], v[10:17], v[202:209], v[66:69]
	v_mfma_f32_16x16x128_f8f6f4 v[58:61], v[2:9], v[202:209], v[58:61]
	v_mfma_f32_16x16x128_f8f6f4 v[50:53], v[10:17], v[210:217], v[50:53]
	v_mfma_f32_16x16x128_f8f6f4 v[42:45], v[2:9], v[210:217], v[42:45]
	s_setprio 2
	s_barrier
	v_mfma_f32_16x16x128_f8f6f4 v[38:41], v[10:17], v[218:225], v[38:41]
	v_mfma_f32_16x16x128_f8f6f4 v[34:37], v[2:9], v[218:225], v[34:37]
	s_setprio 0
	s_nop 0
	s_add_i32 s80, 0, 0x18000
	s_add_i32 s81, 0, 0x1c000
	v_add_u32_e32 v14, s80, v189
	v_add_u32_e32 v30, s81, v189
	ds_read_b128 v[2:5], v14
	ds_read_b128 v[6:9], v14 offset:1024
	ds_read_b128 v[10:13], v14 offset:2048
	ds_read_b128 v[14:17], v14 offset:3072
	ds_read_b128 v[18:21], v30
	ds_read_b128 v[22:25], v30 offset:1024
	ds_read_b128 v[26:29], v30 offset:2048
	ds_read_b128 v[30:33], v30 offset:3072
	s_add_u32 s28, s28, 0xe0000
	s_addc_u32 s29, s29, 0
	s_mov_b32 m0, s62
	v_lshl_add_u64 v[226:227], s[28:29], 0, v[164:165]
	ds_read_b128 v[194:197], v191 offset:32768
	ds_read_b128 v[198:201], v191 offset:33792
	ds_read_b128 v[202:205], v191 offset:34816
	ds_read_b128 v[206:209], v191 offset:35840
	ds_read_b128 v[210:213], v191 offset:36864
	ds_read_b128 v[214:217], v191 offset:37888
	ds_read_b128 v[218:221], v191 offset:38912
	ds_read_b128 v[222:225], v191 offset:39936
	global_load_lds_dwordx4 v[226:227], off
	v_lshl_add_u64 v[226:227], s[28:29], 0, v[166:167]
	s_mov_b32 m0, s63
	s_nop 0
	global_load_lds_dwordx4 v[226:227], off
	s_waitcnt vmcnt(8)
	s_waitcnt lgkmcnt(0)
	s_barrier
	s_setprio 1
	s_waitcnt lgkmcnt(0)
	v_mfma_f32_16x16x128_f8f6f4 v[158:161], v[2:9], v[194:201], v[158:161]
	v_mfma_f32_16x16x128_f8f6f4 v[154:157], v[10:17], v[194:201], v[154:157]
	v_mfma_f32_16x16x128_f8f6f4 v[150:153], v[2:9], v[202:209], v[150:153]
	v_mfma_f32_16x16x128_f8f6f4 v[142:145], v[10:17], v[202:209], v[142:145]
	v_mfma_f32_16x16x128_f8f6f4 v[134:137], v[2:9], v[210:217], v[134:137]
	v_mfma_f32_16x16x128_f8f6f4 v[126:129], v[10:17], v[210:217], v[126:129]
	v_mfma_f32_16x16x128_f8f6f4 v[118:121], v[2:9], v[218:225], v[118:121]
	v_mfma_f32_16x16x128_f8f6f4 v[110:113], v[10:17], v[218:225], v[110:113]
	s_setprio 0
	s_setprio 1
	v_mfma_f32_16x16x128_f8f6f4 v[146:149], v[18:25], v[194:201], v[146:149]
	v_mfma_f32_16x16x128_f8f6f4 v[138:141], v[26:33], v[194:201], v[138:141]
	v_mfma_f32_16x16x128_f8f6f4 v[130:133], v[18:25], v[202:209], v[130:133]
	v_mfma_f32_16x16x128_f8f6f4 v[122:125], v[26:33], v[202:209], v[122:125]
	v_mfma_f32_16x16x128_f8f6f4 v[114:117], v[18:25], v[210:217], v[114:117]
	v_mfma_f32_16x16x128_f8f6f4 v[106:109], v[26:33], v[210:217], v[106:109]
	s_setprio 2
	s_barrier
	v_mfma_f32_16x16x128_f8f6f4 v[102:105], v[18:25], v[218:225], v[102:105]
	v_mfma_f32_16x16x128_f8f6f4 v[98:101], v[26:33], v[218:225], v[98:101]
	s_setprio 0
	s_nop 0
	s_add_i32 s28, s80, s34
	v_lshl_add_u64 v[180:181], v[180:181], 0, s[14:15]
	s_mov_b32 m0, s28
	ds_read_b128 v[194:197], v191 offset:49152
	ds_read_b128 v[198:201], v191 offset:50176
	ds_read_b128 v[202:205], v191 offset:51200
	ds_read_b128 v[206:209], v191 offset:52224
	ds_read_b128 v[210:213], v191 offset:53248
	ds_read_b128 v[214:217], v191 offset:54272
	ds_read_b128 v[218:221], v191 offset:55296
	ds_read_b128 v[222:225], v191 offset:56320
	global_load_lds_dwordx4 v[180:181], off
	v_lshl_add_u64 v[180:181], v[182:183], 0, s[14:15]
	s_add_i32 m0, s28, 0x2000
	v_lshl_add_u64 v[178:179], v[178:179], 0, s[16:17]
	s_add_i32 s28, s81, s34
	global_load_lds_dwordx4 v[180:181], off
	v_lshl_add_u64 v[180:181], v[178:179], 0, v[164:165]
	s_mov_b32 m0, s28
	v_lshl_add_u64 v[178:179], v[178:179], 0, v[166:167]
	global_load_lds_dwordx4 v[180:181], off
	s_add_i32 m0, s28, 0x2000
	s_nop 0
	global_load_lds_dwordx4 v[178:179], off
	v_lshl_add_u64 v[178:179], v[184:185], 0, s[14:15]
	s_mov_b32 m0, s65
	s_nop 0
	global_load_lds_dwordx4 v[178:179], off
	v_lshl_add_u64 v[178:179], v[186:187], 0, s[14:15]
	s_mov_b32 m0, s66
	s_nop 0
	global_load_lds_dwordx4 v[178:179], off
	s_waitcnt vmcnt(8)
	s_waitcnt lgkmcnt(0)
	s_barrier
	s_setprio 1
	s_waitcnt lgkmcnt(0)
	v_mfma_f32_16x16x128_f8f6f4 v[94:97], v[2:9], v[194:201], v[94:97]
	v_mfma_f32_16x16x128_f8f6f4 v[90:93], v[10:17], v[194:201], v[90:93]
	v_mfma_f32_16x16x128_f8f6f4 v[86:89], v[2:9], v[202:209], v[86:89]
	v_mfma_f32_16x16x128_f8f6f4 v[78:81], v[10:17], v[202:209], v[78:81]
	v_mfma_f32_16x16x128_f8f6f4 v[70:73], v[2:9], v[210:217], v[70:73]
	v_mfma_f32_16x16x128_f8f6f4 v[62:65], v[10:17], v[210:217], v[62:65]
	v_mfma_f32_16x16x128_f8f6f4 v[54:57], v[2:9], v[218:225], v[54:57]
	v_mfma_f32_16x16x128_f8f6f4 v[46:49], v[10:17], v[218:225], v[46:49]
	s_setprio 0
	s_setprio 1
	v_mfma_f32_16x16x128_f8f6f4 v[82:85], v[18:25], v[194:201], v[82:85]
	v_mfma_f32_16x16x128_f8f6f4 v[74:77], v[26:33], v[194:201], v[74:77]
	v_mfma_f32_16x16x128_f8f6f4 v[66:69], v[18:25], v[202:209], v[66:69]
	v_mfma_f32_16x16x128_f8f6f4 v[58:61], v[26:33], v[202:209], v[58:61]
	v_mfma_f32_16x16x128_f8f6f4 v[50:53], v[18:25], v[210:217], v[50:53]
	v_mfma_f32_16x16x128_f8f6f4 v[42:45], v[26:33], v[210:217], v[42:45]
	s_setprio 2
	s_barrier
	v_mfma_f32_16x16x128_f8f6f4 v[38:41], v[18:25], v[218:225], v[38:41]
	v_mfma_f32_16x16x128_f8f6f4 v[34:37], v[26:33], v[218:225], v[34:37]
	s_setprio 0
	s_nop 0
	s_add_u32 s26, s26, 0x100
	s_addc_u32 s27, s27, 0
	v_lshl_add_u64 v[176:177], v[176:177], 0, s[22:23]
	s_cmp_ge_u32 s25, s67
	s_mov_b32 s28, s25
	s_cbranch_scc0 .LBB0_2058
	s_and_b64 vcc, exec, s[20:21]
	s_cbranch_vccz .LBB0_2061
	s_barrier
